# v102 + P3: K/V tiles prefetched two steps ahead through two register sets (set B = prologue address registers spilled to spare ring LDS during the step loop); staging block after the QK MFMAs
# baseline (speedup 1.0000x reference)
; __device__ __forceinline__ void attn_phase_mfma(Frame& F) {
;     ...
;         if (grp <= qb) { AT_LOAD_TILE(grp); AT_WRITE_TILE(0); mw = mwn; }
;         if (grp + 2 <= qb) AT_LOAD_TILE(grp + 2);
;         asm volatile("s_waitcnt lgkmcnt(0)" ::: "memory"); __builtin_amdgcn_s_barrier(); asm volatile("" ::: "memory");
;         for (int st = 0; st < nsteps; ++st) {
;     ...
;             if (kt + 2 <= qb) { AT_WRITE_TILE((st + 1) & 1); mw = mwn; }
;             if (kt + 4 <= qb) AT_LOAD_TILE(kt + 4);
.LBB0_549:
	s_add_i32 s0, s14, 64
	s_and_b32 s13, s0, 0xfc0
	v_readlane_b32 s0, v254, 49
	s_waitcnt lgkmcnt(0)
	s_barrier
	v_readlane_b32 s1, v254, 50
	v_mov_b32_e32 v48, v193
	v_mov_b32_e32 v49, v193
	s_waitcnt vmcnt(1)
	v_mov_b64_e32 v[106:107], v[10:11]
	s_waitcnt vmcnt(0)
	v_mov_b64_e32 v[110:111], v[14:15]
	v_mov_b64_e32 v[98:99], v[2:3]
	v_mov_b64_e32 v[102:103], v[6:7]
	v_lshl_add_u64 v[212:213], s[0:1], 0, v[16:17]
	v_mov_b32_e32 v50, v193
	v_mov_b32_e32 v51, v193
	v_mov_b32_e32 v52, v193
	v_mov_b32_e32 v53, v193
	v_mov_b32_e32 v54, v193
	v_mov_b32_e32 v55, v193
	v_mov_b32_e32 v56, v193
	v_mov_b32_e32 v57, v193
	v_mov_b32_e32 v58, v193
	v_mov_b32_e32 v59, v193
	v_mov_b32_e32 v60, v193
	v_mov_b32_e32 v61, v193
	v_mov_b32_e32 v62, v193
	v_mov_b32_e32 v63, v193
	v_mov_b64_e32 v[104:105], v[8:9]
	v_mov_b64_e32 v[108:109], v[12:13]
	v_mov_b64_e32 v[96:97], v[0:1]
	v_mov_b64_e32 v[100:101], v[4:5]
	v_mov_b64_e32 v[32:33], v[48:49]
	v_mov_b64_e32 v[16:17], v[48:49]
	v_mov_b64_e32 v[0:1], v[48:49]
	s_xor_b64 s[6:7], s[2:3], -1
	s_add_i32 s11, s14, 0xffffff62
	s_add_i32 s12, s10, -2
	v_add_u32_e32 v231, s14, v227
	s_mov_b32 s14, 0
	v_mov_b32_e32 v210, 0
	v_mov_b32_e32 v234, 0xff800000
	v_readlane_b32 s15, v253, 31
	v_mov_b64_e32 v[214:215], v[206:207]
	v_mov_b64_e32 v[216:217], v[204:205]
	v_mov_b64_e32 v[218:219], v[202:203]
	v_readlane_b32 s16, v255, 0
	v_mov_b64_e32 v[34:35], v[50:51]
	v_mov_b64_e32 v[36:37], v[52:53]
	v_mov_b64_e32 v[38:39], v[54:55]
	v_mov_b64_e32 v[40:41], v[56:57]
	v_mov_b64_e32 v[42:43], v[58:59]
	v_mov_b64_e32 v[44:45], v[60:61]
	v_mov_b64_e32 v[46:47], v[62:63]
	v_mov_b64_e32 v[18:19], v[50:51]
	v_mov_b64_e32 v[20:21], v[52:53]
	v_mov_b64_e32 v[22:23], v[54:55]
	v_mov_b64_e32 v[24:25], v[56:57]
	v_mov_b64_e32 v[26:27], v[58:59]
	v_mov_b64_e32 v[28:29], v[60:61]
	v_mov_b64_e32 v[30:31], v[62:63]
	v_mov_b64_e32 v[2:3], v[50:51]
	v_mov_b64_e32 v[4:5], v[52:53]
	v_mov_b64_e32 v[6:7], v[54:55]
	v_mov_b64_e32 v[8:9], v[56:57]
	v_mov_b64_e32 v[10:11], v[58:59]
	v_mov_b64_e32 v[12:13], v[60:61]
	v_mov_b64_e32 v[14:15], v[62:63]
	v_readlane_b32 s36, v253, 16
	v_mbcnt_lo_u32_b32 v197, -1, 0
	v_mbcnt_hi_u32_b32 v197, -1, v197
	s_lshl_b32 s36, s36, 4
	s_add_i32 s36, s36, 0x13000
	v_lshl_add_u32 v197, v197, 4, s36
	ds_write_b128 v197, v[176:179]
	ds_write_b128 v197, v[180:183] offset:8192
	ds_write_b128 v197, v[184:187] offset:16384
	ds_write_b128 v197, v[188:191] offset:24576
	s_add_i32 s36, s15, 4
	s_cmp_gt_u32 s36, s10
	s_cbranch_scc1 .Lp3d_pro_noload
	v_lshl_add_u64 v[82:83], s[26:27], 0, v[212:213]
	global_load_dword v196, v[82:83], off
	v_lshl_add_u64 v[82:83], s[26:27], 0, v[214:215]
	v_lshl_add_u64 v[84:85], s[26:27], 0, v[216:217]
	global_load_dwordx4 v[176:179], v[82:83], off
	global_load_dwordx4 v[180:183], v[84:85], off
	v_lshl_add_u64 v[82:83], s[26:27], 0, v[218:219]
	v_add_co_u32_e32 v84, vcc, 0xa902000, v82
	s_nop 1
	v_addc_co_u32_e32 v85, vcc, 0, v83, vcc
	v_add_co_u32_e32 v82, vcc, 0xa906000, v82
	s_nop 1
	v_addc_co_u32_e32 v83, vcc, 0, v83, vcc
	global_load_dwordx4 v[184:187], v[84:85], off offset:2560
	global_load_dwordx4 v[188:191], v[82:83], off
.Lp3d_pro_noload:
	s_mov_b32 s17, 0
	s_and_b32 s18, s17, 1
	s_cmp_gt_u32 s15, s10
	s_cbranch_scc1 .LBB0_555
.LBB0_550:
	s_mul_i32 s0, s18, 0x2200
	v_add_u32_e32 v68, s0, v221
	ds_read_b128 v[64:67], v68
	ds_read_b128 v[80:83], v68 offset:32
	ds_read_b128 v[84:87], v68 offset:64
	ds_read_b128 v[88:91], v68 offset:96
	ds_read_b128 v[92:95], v68 offset:128
	ds_read_b128 v[144:147], v68 offset:160
	ds_read_b128 v[148:151], v68 offset:192
	ds_read_b128 v[152:155], v68 offset:224
	s_waitcnt lgkmcnt(7)
	v_mfma_f32_32x32x16_bf16 v[64:79], v[64:67], v[136:139], 0
	s_mul_i32 s0, s18, 0x2400
	s_waitcnt lgkmcnt(6)
	v_mfma_f32_32x32x16_bf16 v[64:79], v[80:83], v[112:115], v[64:79]
	v_add_u32_e32 v80, s0, v226
	v_add_u32_e32 v81, 0x8800, v80
	s_waitcnt lgkmcnt(5)
	v_mfma_f32_32x32x16_bf16 v[64:79], v[84:87], v[116:119], v[64:79]
	s_waitcnt lgkmcnt(4)
	v_mfma_f32_32x32x16_bf16 v[64:79], v[88:91], v[120:123], v[64:79]
	s_waitcnt lgkmcnt(3)
	v_mfma_f32_32x32x16_bf16 v[64:79], v[92:95], v[124:127], v[64:79]
	s_waitcnt lgkmcnt(2)
	v_mfma_f32_32x32x16_bf16 v[64:79], v[144:147], v[128:131], v[64:79]
	s_waitcnt lgkmcnt(1)
	v_mfma_f32_32x32x16_bf16 v[64:79], v[148:151], v[132:135], v[64:79]
	ds_read2_b64 v[148:151], v81 offset1:2
	ds_read2_b64 v[144:147], v81 offset0:4 offset1:6
	v_add_u32_e32 v81, 0x9000, v80
	s_waitcnt lgkmcnt(2)
	v_mfma_f32_32x32x16_bf16 v[64:79], v[152:155], v[140:143], v[64:79]
	ds_read2_b64 v[152:155], v81 offset0:32 offset1:34
	ds_read2_b64 v[156:159], v81 offset0:36 offset1:38
	v_add_u32_e32 v81, 0x9800, v80
	v_add_u32_e32 v80, 0xa000, v80
	ds_read2_b64 v[164:167], v81 offset0:64 offset1:66
	ds_read2_b64 v[168:171], v81 offset0:68 offset1:70
	ds_read2_b64 v[172:175], v80 offset0:96 offset1:98
	ds_read2_b64 v[160:163], v80 offset0:100 offset1:102
	v_lshrrev_b32_e32 v233, v222, v229
	v_and_b32_e32 v199, 1, v233
	v_and_b32_e32 v198, 2, v233
	v_and_b32_e32 v242, 4, v233
	v_and_b32_e32 v250, 8, v233
	v_and_b32_e32 v249, 0x100, v233
	v_and_b32_e32 v248, 0x200, v233
	v_and_b32_e32 v244, 0x400, v233
	v_and_b32_e32 v243, 0x800, v233
	v_and_b32_e32 v241, 0x10000, v233
	v_and_b32_e32 v240, 0x20000, v233
	v_and_b32_e32 v239, 0x40000, v233
	v_and_b32_e32 v238, 0x80000, v233
	v_and_b32_e32 v237, 0x1000000, v233
	v_and_b32_e32 v236, 0x2000000, v233
	v_and_b32_e32 v235, 0x4000000, v233
	s_cmp_gt_i32 s15, s12
	s_cbranch_scc1 .Lp3d_m_nowrite
	s_add_i32 s36, s15, 4
	s_cmp_gt_u32 s36, s10
	s_cbranch_scc1 .Lp3d_m_wlast
	s_waitcnt vmcnt(5)
	s_branch .Lp3d_m_wgo

; __device__ __forceinline__ void attn_phase_mfma(Frame& F) {
;     ...
;             if (kt + 2 <= qb) { AT_WRITE_TILE((st + 1) & 1); mw = mwn; }
;             if (kt + 4 <= qb) AT_LOAD_TILE(kt + 4);
.Lp3d_m_wgo:
	s_cmp_eq_u32 s18, 0
	s_cbranch_scc0 .Lp3d_m_wB
	s_xor_b32 s36, s18, 1
	s_mul_i32 s37, s36, 0x2200
	s_mulk_i32 s36, 0x2400
	v_add_u32_e32 v82, s37, v224
	ds_write_b128 v82, v[96:99]
	ds_write_b128 v82, v[100:103] offset:4352
	v_add_u32_e32 v83, s36, v225
	v_add_u32_e32 v83, 0x8800, v83
	v_and_b32_e32 v82, 0xffff, v104
	v_lshrrev_b32_e32 v84, 16, v104
	v_lshl_or_b32 v82, v108, 16, v82
	v_and_or_b32 v84, v108, s92, v84
	ds_write2_b32 v83, v82, v84 offset1:18
	v_and_b32_e32 v82, 0xffff, v105
	v_lshrrev_b32_e32 v84, 16, v105
	v_lshl_or_b32 v82, v109, 16, v82
	v_and_or_b32 v84, v109, s92, v84
	ds_write2_b32 v83, v82, v84 offset0:36 offset1:54
	v_and_b32_e32 v82, 0xffff, v106
	v_lshrrev_b32_e32 v84, 16, v106
	v_lshl_or_b32 v82, v110, 16, v82
	v_and_or_b32 v84, v110, s92, v84
	ds_write2_b32 v83, v82, v84 offset0:72 offset1:90
	v_and_b32_e32 v82, 0xffff, v107
	v_lshrrev_b32_e32 v84, 16, v107
	v_lshl_or_b32 v82, v111, 16, v82
	v_and_or_b32 v84, v111, s92, v84
	ds_write2_b32 v83, v82, v84 offset0:108 offset1:126
	v_mov_b32_e32 v229, v230
	s_branch .Lp3d_m_nowrite
.Lp3d_m_wB:
	s_xor_b32 s36, s18, 1
	s_mul_i32 s37, s36, 0x2200
	s_mulk_i32 s36, 0x2400
	v_add_u32_e32 v82, s37, v224
	ds_write_b128 v82, v[176:179]
	ds_write_b128 v82, v[180:183] offset:4352
	v_add_u32_e32 v83, s36, v225
	v_add_u32_e32 v83, 0x8800, v83
	v_and_b32_e32 v82, 0xffff, v184
	v_lshrrev_b32_e32 v84, 16, v184
	v_lshl_or_b32 v82, v188, 16, v82
	v_and_or_b32 v84, v188, s92, v84
	ds_write2_b32 v83, v82, v84 offset1:18
	v_and_b32_e32 v82, 0xffff, v185
	v_lshrrev_b32_e32 v84, 16, v185
	v_lshl_or_b32 v82, v189, 16, v82
	v_and_or_b32 v84, v189, s92, v84
	ds_write2_b32 v83, v82, v84 offset0:36 offset1:54
	v_and_b32_e32 v82, 0xffff, v186
	v_lshrrev_b32_e32 v84, 16, v186
	v_lshl_or_b32 v82, v190, 16, v82
	v_and_or_b32 v84, v190, s92, v84
	ds_write2_b32 v83, v82, v84 offset0:72 offset1:90
	v_and_b32_e32 v82, 0xffff, v187
	v_lshrrev_b32_e32 v84, 16, v187
	v_lshl_or_b32 v82, v191, 16, v82
	v_and_or_b32 v84, v191, s92, v84
	ds_write2_b32 v83, v82, v84 offset0:108 offset1:126
	v_mov_b32_e32 v229, v196
.Lp3d_m_nowrite:
	s_add_i32 s36, s15, 6
	s_cmp_gt_u32 s36, s10
	s_cbranch_scc1 .Lp3d_m_noload
	s_cmp_eq_u32 s18, 0
	s_cbranch_scc0 .Lp3d_m_lB
	s_mov_b64 s[36:37], 0xd8000
	v_lshl_add_u64 v[82:83], s[26:27], 0, v[212:213]
	global_load_dword v230, v[82:83], off offset:8
	v_lshl_add_u64 v[82:83], s[26:27], 0, v[214:215]
	v_lshl_add_u64 v[84:85], s[26:27], 0, v[216:217]
	v_lshl_add_u64 v[82:83], v[82:83], 0, s[36:37]
	v_lshl_add_u64 v[84:85], v[84:85], 0, s[36:37]
	global_load_dwordx4 v[96:99], v[82:83], off
	global_load_dwordx4 v[100:103], v[84:85], off
	v_lshl_add_u64 v[82:83], s[26:27], 0, v[218:219]
	v_lshl_add_u64 v[82:83], v[82:83], 0, s[36:37]
	v_add_co_u32_e32 v84, vcc, 0xa902000, v82
	s_nop 1
	v_addc_co_u32_e32 v85, vcc, 0, v83, vcc
	v_add_co_u32_e32 v82, vcc, 0xa906000, v82
	s_nop 1
	v_addc_co_u32_e32 v83, vcc, 0, v83, vcc
	global_load_dwordx4 v[104:107], v[84:85], off offset:2560
	global_load_dwordx4 v[108:111], v[82:83], off
	s_branch .Lp3d_m_noload
.Lp3d_m_lB:
	s_mov_b64 s[36:37], 0xd8000
	v_lshl_add_u64 v[82:83], s[26:27], 0, v[212:213]
	global_load_dword v196, v[82:83], off offset:8
	v_lshl_add_u64 v[82:83], s[26:27], 0, v[214:215]
	v_lshl_add_u64 v[84:85], s[26:27], 0, v[216:217]
	v_lshl_add_u64 v[82:83], v[82:83], 0, s[36:37]
	v_lshl_add_u64 v[84:85], v[84:85], 0, s[36:37]
	global_load_dwordx4 v[176:179], v[82:83], off
	global_load_dwordx4 v[180:183], v[84:85], off
	v_lshl_add_u64 v[82:83], s[26:27], 0, v[218:219]
	v_lshl_add_u64 v[82:83], v[82:83], 0, s[36:37]
	v_add_co_u32_e32 v84, vcc, 0xa902000, v82
	s_nop 1
	v_addc_co_u32_e32 v85, vcc, 0, v83, vcc
	v_add_co_u32_e32 v82, vcc, 0xa906000, v82
	s_nop 1
	v_addc_co_u32_e32 v83, vcc, 0, v83, vcc
	global_load_dwordx4 v[184:187], v[84:85], off offset:2560
	global_load_dwordx4 v[188:191], v[82:83], off

; #define LAS __attribute__((address_space(3)))
; __device__ __forceinline__ void attn_phase_mfma(Frame& F) {
;     ...
;         for (int st = 0; st < nsteps; ++st) {
;             const int kt = 2 * st + grp; const bool valid = kt <= qb;
;             LAS unsigned char* KB = KB0 + (st & 1) * (32 * AT_KPITCH); LAS unsigned char* VB = VB0 + (st & 1) * (128 * AT_VPITCH);
;             if (valid) {
;     ...
;             if (kt + 2 <= qb) { AT_WRITE_TILE((st + 1) & 1); mw = mwn; }
.LBB0_555:
	v_mov_b32_e32 v232, v234
	s_cmp_gt_i32 s15, s12
	s_cbranch_scc1 .Lp3d_i_nowrite
	s_add_i32 s0, s15, 4
	s_cmp_gt_u32 s0, s10
	s_cbranch_scc1 .Lp3d_i_wlast
	s_waitcnt vmcnt(5)
	s_branch .Lp3d_i_wgo

; __device__ __forceinline__ void attn_phase_mfma(Frame& F) {
;     ...
;             if (kt + 2 <= qb) { AT_WRITE_TILE((st + 1) & 1); mw = mwn; }
;             if (kt + 4 <= qb) AT_LOAD_TILE(kt + 4);
;             asm volatile("s_waitcnt lgkmcnt(0)" ::: "memory"); __builtin_amdgcn_s_barrier(); asm volatile("" ::: "memory");
;         }
.Lp3d_i_wgo:
	s_cmp_eq_u32 s18, 0
	s_cbranch_scc0 .Lp3d_i_wB
	s_xor_b32 s0, s18, 1
	s_mul_i32 s1, s0, 0x2200
	s_mulk_i32 s0, 0x2400
	v_add_u32_e32 v64, s1, v224
	ds_write_b128 v64, v[96:99]
	ds_write_b128 v64, v[100:103] offset:4352
	v_add_u32_e32 v65, s0, v225
	v_add_u32_e32 v65, 0x8800, v65
	v_and_b32_e32 v64, 0xffff, v104
	v_lshrrev_b32_e32 v66, 16, v104
	v_lshl_or_b32 v64, v108, 16, v64
	v_and_or_b32 v66, v108, s92, v66
	ds_write2_b32 v65, v64, v66 offset1:18
	v_and_b32_e32 v64, 0xffff, v105
	v_lshrrev_b32_e32 v66, 16, v105
	v_lshl_or_b32 v64, v109, 16, v64
	v_and_or_b32 v66, v109, s92, v66
	ds_write2_b32 v65, v64, v66 offset0:36 offset1:54
	v_and_b32_e32 v64, 0xffff, v106
	v_lshrrev_b32_e32 v66, 16, v106
	v_lshl_or_b32 v64, v110, 16, v64
	v_and_or_b32 v66, v110, s92, v66
	ds_write2_b32 v65, v64, v66 offset0:72 offset1:90
	v_and_b32_e32 v64, 0xffff, v107
	v_lshrrev_b32_e32 v66, 16, v107
	v_lshl_or_b32 v64, v111, 16, v64
	v_and_or_b32 v66, v111, s92, v66
	ds_write2_b32 v65, v64, v66 offset0:108 offset1:126
	v_mov_b32_e32 v229, v230
	s_branch .Lp3d_i_nowrite
.Lp3d_i_wB:
	s_xor_b32 s0, s18, 1
	s_mul_i32 s1, s0, 0x2200
	s_mulk_i32 s0, 0x2400
	v_add_u32_e32 v64, s1, v224
	ds_write_b128 v64, v[176:179]
	ds_write_b128 v64, v[180:183] offset:4352
	v_add_u32_e32 v65, s0, v225
	v_add_u32_e32 v65, 0x8800, v65
	v_and_b32_e32 v64, 0xffff, v184
	v_lshrrev_b32_e32 v66, 16, v184
	v_lshl_or_b32 v64, v188, 16, v64
	v_and_or_b32 v66, v188, s92, v66
	ds_write2_b32 v65, v64, v66 offset1:18
	v_and_b32_e32 v64, 0xffff, v185
	v_lshrrev_b32_e32 v66, 16, v185
	v_lshl_or_b32 v64, v189, 16, v64
	v_and_or_b32 v66, v189, s92, v66
	ds_write2_b32 v65, v64, v66 offset0:36 offset1:54
	v_and_b32_e32 v64, 0xffff, v186
	v_lshrrev_b32_e32 v66, 16, v186
	v_lshl_or_b32 v64, v190, 16, v64
	v_and_or_b32 v66, v190, s92, v66
	ds_write2_b32 v65, v64, v66 offset0:72 offset1:90
	v_and_b32_e32 v64, 0xffff, v187
	v_lshrrev_b32_e32 v66, 16, v187
	v_lshl_or_b32 v64, v191, 16, v64
	v_and_or_b32 v66, v191, s92, v66
	ds_write2_b32 v65, v64, v66 offset0:108 offset1:126
	v_mov_b32_e32 v229, v196
.Lp3d_i_nowrite:
	s_add_i32 s0, s15, 6
	s_cmp_gt_u32 s0, s10
	s_cbranch_scc1 .Lp3d_i_noload
	s_cmp_eq_u32 s18, 0
	s_cbranch_scc0 .Lp3d_i_lB
	s_mov_b64 s[0:1], 0xd8000
	v_lshl_add_u64 v[64:65], s[26:27], 0, v[212:213]
	global_load_dword v230, v[64:65], off offset:8
	v_lshl_add_u64 v[64:65], s[26:27], 0, v[214:215]
	v_lshl_add_u64 v[66:67], s[26:27], 0, v[216:217]
	v_lshl_add_u64 v[64:65], v[64:65], 0, s[0:1]
	v_lshl_add_u64 v[66:67], v[66:67], 0, s[0:1]
	global_load_dwordx4 v[96:99], v[64:65], off
	global_load_dwordx4 v[100:103], v[66:67], off
	v_lshl_add_u64 v[64:65], s[26:27], 0, v[218:219]
	v_lshl_add_u64 v[64:65], v[64:65], 0, s[0:1]
	v_add_co_u32_e32 v66, vcc, 0xa902000, v64
	s_nop 1
	v_addc_co_u32_e32 v67, vcc, 0, v65, vcc
	v_add_co_u32_e32 v64, vcc, 0xa906000, v64
	s_nop 1
	v_addc_co_u32_e32 v65, vcc, 0, v65, vcc
	global_load_dwordx4 v[104:107], v[66:67], off offset:2560
	global_load_dwordx4 v[108:111], v[64:65], off
	s_branch .Lp3d_i_noload
.Lp3d_i_lB:
	s_mov_b64 s[0:1], 0xd8000
	v_lshl_add_u64 v[64:65], s[26:27], 0, v[212:213]
	global_load_dword v196, v[64:65], off offset:8
	v_lshl_add_u64 v[64:65], s[26:27], 0, v[214:215]
	v_lshl_add_u64 v[66:67], s[26:27], 0, v[216:217]
	v_lshl_add_u64 v[64:65], v[64:65], 0, s[0:1]
	v_lshl_add_u64 v[66:67], v[66:67], 0, s[0:1]
	global_load_dwordx4 v[176:179], v[64:65], off
	global_load_dwordx4 v[180:183], v[66:67], off
	v_lshl_add_u64 v[64:65], s[26:27], 0, v[218:219]
	v_lshl_add_u64 v[64:65], v[64:65], 0, s[0:1]
	v_add_co_u32_e32 v66, vcc, 0xa902000, v64
	s_nop 1
	v_addc_co_u32_e32 v67, vcc, 0, v65, vcc
	v_add_co_u32_e32 v64, vcc, 0xa906000, v64
	s_nop 1
	v_addc_co_u32_e32 v65, vcc, 0, v65, vcc
	global_load_dwordx4 v[184:187], v[66:67], off offset:2560
	global_load_dwordx4 v[188:191], v[64:65], off
.Lp3d_i_noload:
.LBB0_559:
	s_waitcnt lgkmcnt(0)
	s_barrier
	s_sub_i32 s14, s14, 64
	s_add_i32 s17, s17, 1
	s_add_i32 s0, s13, s14
	s_add_i32 s16, s16, 64
	s_mov_b64 s[2:3], 0xd8000
	s_add_i32 s15, s15, 2
	v_lshl_add_u64 v[212:213], v[212:213], 0, 8
	v_lshl_add_u64 v[218:219], v[218:219], 0, s[2:3]
	v_lshl_add_u64 v[216:217], v[216:217], 0, s[2:3]
	s_cmp_eq_u32 s0, 0
	v_lshl_add_u64 v[214:215], v[214:215], 0, s[2:3]
	s_cbranch_scc1 .LBB0_563
	v_mov_b32_e32 v234, v232
	s_and_b32 s18, s17, 1
	s_cmp_gt_u32 s15, s10
	s_cbranch_scc1 .LBB0_555
	s_branch .LBB0_550

; __device__ __forceinline__ void attn_phase_mfma(Frame& F) {
;     ...
;         if (grp == 1) {
; #pragma unroll
;             for (int db = 0; db < 4; ++db)
; #pragma unroll
;                 for (int r = 0; r < 16; ++r) MG[(db * 16 + r) * 64 + lane] = o[db][r];
;             MG[64 * 64 + lane] = m; MG[65 * 64 + lane] = l;
;         }
.LBB0_563:
	v_readlane_b32 s36, v253, 16
	v_mbcnt_lo_u32_b32 v197, -1, 0
	v_mbcnt_hi_u32_b32 v197, -1, v197
	s_lshl_b32 s36, s36, 4
	s_add_i32 s36, s36, 0x13000
	v_lshl_add_u32 v197, v197, 4, s36
	ds_read_b128 v[176:179], v197
	ds_read_b128 v[180:183], v197 offset:8192
	ds_read_b128 v[184:187], v197 offset:16384
	ds_read_b128 v[188:191], v197 offset:24576
	s_waitcnt lgkmcnt(0)
	v_readlane_b32 s0, v253, 32
	v_readlane_b32 s1, v253, 33
	s_andn2_b64 vcc, exec, s[0:1]
	s_cbranch_vccnz .LBB0_565
	ds_write2st64_b32 v223, v48, v49 offset1:1
	ds_write2st64_b32 v223, v50, v51 offset0:2 offset1:3
	ds_write2st64_b32 v223, v52, v53 offset0:4 offset1:5
	ds_write2st64_b32 v223, v54, v55 offset0:6 offset1:7
	ds_write2st64_b32 v223, v56, v57 offset0:8 offset1:9
	ds_write2st64_b32 v223, v58, v59 offset0:10 offset1:11
	ds_write2st64_b32 v223, v60, v61 offset0:12 offset1:13
	ds_write2st64_b32 v223, v62, v63 offset0:14 offset1:15
	ds_write2st64_b32 v223, v32, v33 offset0:16 offset1:17
	ds_write2st64_b32 v223, v34, v35 offset0:18 offset1:19
	ds_write2st64_b32 v223, v36, v37 offset0:20 offset1:21
	ds_write2st64_b32 v223, v38, v39 offset0:22 offset1:23
	ds_write2st64_b32 v223, v40, v41 offset0:24 offset1:25
	ds_write2st64_b32 v223, v42, v43 offset0:26 offset1:27
	ds_write2st64_b32 v223, v44, v45 offset0:28 offset1:29
	ds_write2st64_b32 v223, v46, v47 offset0:30 offset1:31
	ds_write2st64_b32 v223, v16, v17 offset0:32 offset1:33
	ds_write2st64_b32 v223, v18, v19 offset0:34 offset1:35
	ds_write2st64_b32 v223, v20, v21 offset0:36 offset1:37
	ds_write2st64_b32 v223, v22, v23 offset0:38 offset1:39
	ds_write2st64_b32 v223, v24, v25 offset0:40 offset1:41
	ds_write2st64_b32 v223, v26, v27 offset0:42 offset1:43
	ds_write2st64_b32 v223, v28, v29 offset0:44 offset1:45
	ds_write2st64_b32 v223, v30, v31 offset0:46 offset1:47
	ds_write2st64_b32 v223, v0, v1 offset0:48 offset1:49
	ds_write2st64_b32 v223, v2, v3 offset0:50 offset1:51
	ds_write2st64_b32 v223, v4, v5 offset0:52 offset1:53
	ds_write2st64_b32 v223, v6, v7 offset0:54 offset1:55
	ds_write2st64_b32 v223, v8, v9 offset0:56 offset1:57
	ds_write2st64_b32 v223, v10, v11 offset0:58 offset1:59
	ds_write2st64_b32 v223, v12, v13 offset0:60 offset1:61
	ds_write2st64_b32 v223, v14, v15 offset0:62 offset1:63
	ds_write2st64_b32 v223, v232, v210 offset0:64 offset1:65
